# schedule: in_proj spare workgroups convert almost nothing (60 / 10 blocks), out_proj layer-0 spare workgroups 1000, mixer phases 2537 per layer
# baseline (speedup 1.0000x reference)
.LBB0_310:
	s_lshl_b32 s4, s2, 3
	v_writelane_b32 v254, s4, 7
	s_lshl_b32 s4, s3, 3
	v_writelane_b32 v254, s4, 8
	s_lshl_b32 s4, s2, 9
	s_lshl_b32 s62, s3, 9
	s_cmp_eq_u32 s2, 0
	v_writelane_b32 v254, s4, 9
	s_cselect_b64 s[4:5], -1, 0
	v_writelane_b32 v254, s4, 10
	s_lshl_b32 s8, s2, 5
	s_and_b32 s14, s87, 31
	v_writelane_b32 v254, s5, 11
	s_mul_i32 s4, s2, 0x6b
	s_add_i32 s7, s4, 0xffffd954
	s_ashr_i32 s11, s87, 5
	s_lshl_b32 s4, s2, 4
	s_lshl_b32 s66, s3, 4
	s_cmpk_lt_i32 s2, 0x100
	v_writelane_b32 v254, s4, 12
	s_cselect_b64 s[4:5], -1, 0
	v_writelane_b32 v254, s4, 13
	s_movk_i32 s64, 0x80
	s_movk_i32 s65, 0xff00
	v_writelane_b32 v254, s5, 14
	s_lshr_b32 s4, s2, 3
	s_mul_i32 s4, s4, 5
	s_and_b32 s5, s2, 7
	s_add_i32 s4, s4, s5
	s_add_i32 s4, s4, -3
	s_cmp_lt_u32 s5, 3
	s_cselect_b32 s4, 0x7fff, s4
	s_cmpk_lt_i32 s4, 0x80
	v_writelane_b32 v254, s4, 15
	s_cselect_b64 s[4:5], -1, 0
	s_and_b32 s9, s87, 3
	v_writelane_b32 v254, s4, 16
	s_cmpk_lt_i32 s2, 0x200
	s_movk_i32 s56, 0x1000
	v_writelane_b32 v254, s5, 17
	s_cselect_b64 s[4:5], -1, 0
	v_writelane_b32 v254, s4, 18
	s_lshl_b32 s74, s3, 5
	s_movk_i32 s77, 0x4400
	v_writelane_b32 v254, s5, 19
	s_lshl_b32 s4, s2, 2
	s_and_b32 s4, s4, 0xffffff00
	v_writelane_b32 v254, s4, 20
	s_lshl_b32 s4, s2, 6
	s_and_b32 s6, s4, 0xfc0
	s_cmp_gt_i32 s3, 0
	v_writelane_b32 v254, s4, 21
	s_cselect_b64 s[4:5], -1, 0
	v_writelane_b32 v254, s4, 22
	s_ashr_i32 s12, s87, 2
	s_mov_b32 s10, s12
	v_writelane_b32 v254, s5, 23
	s_ashr_i32 s4, s87, 3
	v_writelane_b32 v254, s4, 24
	s_and_b32 s5, s87, 7
	s_lshl_b32 s4, s5, 7
	v_writelane_b32 v254, s5, 25
	s_lshl_b32 s5, s5, 18
	v_writelane_b32 v254, s5, 26
	s_ashr_i32 s13, s12, 31
	v_writelane_b32 v254, s10, 27
	s_lshl_b64 s[12:13], s[12:13], 18
	s_lshl_b32 s5, s9, 8
	v_writelane_b32 v254, s11, 28
	v_writelane_b32 v254, s12, 29
	s_mov_b32 s38, 0x78787879
	s_movk_i32 s39, 0xef00
	v_writelane_b32 v254, s13, 30
	v_writelane_b32 v254, s9, 31
	s_lshl_b32 s9, s9, 18
	s_cmpk_lt_i32 s2, 0x84
	v_writelane_b32 v254, s9, 32
	s_cselect_b32 s9, 32, 0x6b
	v_writelane_b32 v254, s9, 33
	v_writelane_b32 v254, s8, 34
	s_cselect_b32 s7, s8, s7
	v_writelane_b32 v254, s7, 35
	s_add_i32 s7, s3, -1
	s_cmp_gt_u32 s7, 6
	s_cselect_b64 s[8:9], -1, 0
	s_abs_i32 s12, s3
	v_cvt_f32_u32_e32 v1, s12
	v_writelane_b32 v254, s8, 36
	s_sub_i32 s7, 0, s12
	s_and_b32 s76, s3, 0x7ffffff8
	v_rcp_iflag_f32_e32 v1, v1
	v_writelane_b32 v254, s9, 37
	s_ashr_i32 s13, s3, 31
	s_mov_b32 s59, 0x800000
	v_mul_f32_e32 v1, 0x4f7ffffe, v1
	v_cvt_u32_f32_e32 v1, v1
	v_mov_b32_e32 v205, 1
	v_mov_b32_e32 v221, 0x1400
	v_mov_b32_e32 v204, 0x20200
	v_readfirstlane_b32 s8, v1
	s_mul_i32 s7, s7, s8
	s_mul_hi_u32 s7, s8, s7
	s_add_i32 s7, s8, s7
	v_writelane_b32 v254, s7, 38
	s_mul_hi_u32 s7, s7, 0x9e9
	s_mul_i32 s8, s7, s12
	s_sub_i32 s8, 0x9e9, s8
	s_add_i32 s9, s7, 1
	s_sub_i32 s10, s8, s12
	s_cmp_ge_u32 s8, s12
	s_cselect_b32 s7, s9, s7
	s_cselect_b32 s8, s10, s8
	s_add_i32 s9, s7, 1
	s_cmp_ge_u32 s8, s12
	s_cselect_b32 s7, s9, s7
	s_xor_b32 s7, s7, s13
	s_sub_i32 s7, s7, s13
	s_mul_i32 s8, s7, s3
	s_sub_i32 s8, 0x9e9, s8
	s_mul_i32 s9, s7, s87
	s_min_i32 s10, s87, s8
	v_writelane_b32 v254, s12, 39
	s_add_i32 s9, s9, s10
	v_writelane_b32 v254, s13, 40
	s_cmp_lt_i32 s87, s8
	v_writelane_b32 v254, s9, 41
	s_cselect_b64 s[8:9], -1, 0
	s_cmp_lg_u64 s[8:9], 0
	s_addc_u32 s7, s7, 0
	v_writelane_b32 v254, s7, 42
	s_lshl_b32 s7, s3, 1
	v_writelane_b32 v254, s7, 43
	s_add_i32 s7, s11, 17
	v_writelane_b32 v254, s7, 44
	s_lshl_b32 s7, s7, 4
	v_writelane_b32 v254, s7, 45
	s_lshl_b32 s7, s14, 4
	v_writelane_b32 v254, s14, 46
	s_add_i32 s8, s7, 0xded0
	v_writelane_b32 v254, s8, 47
	s_add_i32 s8, s11, 9
	v_writelane_b32 v254, s8, 48
	s_lshl_b32 s8, s8, 4
	v_writelane_b32 v254, s8, 49
	v_writelane_b32 v254, s11, 50
	s_add_i32 s8, s11, 1
	v_writelane_b32 v254, s8, 51
	s_or_b32 s8, s7, 0xfffffe00
	v_writelane_b32 v254, s8, 52
	s_lshl_b32 s8, s3, 6
	v_writelane_b32 v254, s8, 53
	s_add_i32 s7, s7, 0xa050
	v_writelane_b32 v254, s7, 54
	s_add_i32 s7, 0, 0x12000
	v_writelane_b32 v254, s7, 55
	s_add_i32 s7, 0, 0x27020
	v_writelane_b32 v254, s7, 56
	s_add_i32 s7, 0, 0x27024
	v_writelane_b32 v254, s7, 57
	s_add_i32 s7, 0, 0x25000
	v_writelane_b32 v254, s7, 58
	s_lshl_b32 s6, s6, 1
	v_writelane_b32 v254, s6, 59
	s_lshl_b32 s5, s5, 2
	v_writelane_b32 v254, s5, 60
	s_add_i32 s5, 0, 0x25400
	v_writelane_b32 v254, s5, 61
	s_add_i32 s5, 0, 0x10200
	v_writelane_b32 v254, s5, 62
	s_add_i32 s5, 0, 0x20100
	v_writelane_b32 v254, s5, 63
	s_add_i32 s5, 0, 0x20010
	v_writelane_b32 v255, s5, 0
	s_add_i32 s5, 0, 0x20110
	v_writelane_b32 v255, s5, 1
	s_add_i32 s5, 0, 0x20020
	v_writelane_b32 v255, s5, 2
	s_add_i32 s5, 0, 0x20120
	v_writelane_b32 v255, s5, 3
	s_add_i32 s5, 0, 0x20030
	v_writelane_b32 v255, s5, 4
	s_add_i32 s5, 0, 0x20130
	v_writelane_b32 v255, s5, 5
	s_add_i32 s5, 0, 0x20040
	v_writelane_b32 v255, s5, 6
	s_add_i32 s5, 0, 0x20140
	v_writelane_b32 v255, s5, 7
	s_add_i32 s5, 0, 0x20050
	v_writelane_b32 v255, s5, 8
	s_add_i32 s5, 0, 0x20150
	v_writelane_b32 v255, s5, 9
	s_add_i32 s5, 0, 0x20060
	v_writelane_b32 v255, s5, 10
	s_add_i32 s5, 0, 0x20160
	v_writelane_b32 v255, s5, 11
	s_add_i32 s5, 0, 0x20070
	v_writelane_b32 v255, s5, 12
	s_add_i32 s5, 0, 0x20170
	v_writelane_b32 v255, s5, 13
	s_add_i32 s5, 0, 0x20180
	v_writelane_b32 v255, s5, 14
	s_add_i32 s5, 0, 0x20084
	v_writelane_b32 v255, s5, 15
	s_add_i32 s5, 0, 0x20024
	v_writelane_b32 v255, s5, 16
	s_add_i32 s5, 0, 0x2002c
	v_writelane_b32 v255, s5, 17
	s_add_i32 s5, 0, 0x20034
	v_writelane_b32 v255, s5, 18
	s_add_i32 s5, 0, 0x2003c
	v_writelane_b32 v255, s5, 19
	s_add_i32 s5, 0, 0x20044
	v_writelane_b32 v255, s5, 20
	s_add_i32 s5, 0, 0x2004c
	v_writelane_b32 v255, s5, 21
	s_add_i32 s5, 0, 0x20054
	v_writelane_b32 v255, s5, 22
	s_add_i32 s5, 0, 0x2005c
	v_writelane_b32 v255, s5, 23
	s_add_i32 s5, 0, 0x20064
	v_writelane_b32 v255, s5, 24
	s_add_i32 s5, 0, 0x2006c
	v_writelane_b32 v255, s5, 25
	s_add_i32 s5, 0, 0x20074
	v_writelane_b32 v255, s5, 26
	s_add_i32 s5, 0, 0x2007c
	v_writelane_b32 v255, s5, 27
	s_add_i32 s5, 0, 0x20800
	v_writelane_b32 v255, s5, 28
	s_lshl_b32 s4, s4, 2
	v_writelane_b32 v255, s4, 29
	s_ashr_i32 s63, s62, 31
	s_ashr_i32 s67, s66, 31
	v_writelane_b32 v255, s5, 30
	v_cmp_eq_u32_e64 s[4:5], 0, v0
	s_mov_b32 s6, s74
	s_add_i32 s84, 0, 0x20004
	v_writelane_b32 v255, s4, 31
	s_add_i32 s69, 0, 0x2000c
	s_add_i32 s68, 0, 0x20014
	v_writelane_b32 v255, s5, 32
	s_lshl_b64 s[4:5], s[62:63], 2
	v_writelane_b32 v255, s4, 33
	s_add_i32 s49, 0, 0x2001c
	v_mov_b32_e32 v1, 0
	v_writelane_b32 v255, s5, 34
	s_lshl_b64 s[4:5], s[66:67], 12
	v_writelane_b32 v255, s4, 35
	v_mov_b32_e32 v220, 0xff800000
	s_movk_i32 s47, 0x3ff
	v_writelane_b32 v255, s5, 36
	v_writelane_b32 v255, s6, 37
	s_mov_b32 s83, 0x34400000
	s_mov_b32 s80, 0x36500000
	v_writelane_b32 v255, s7, 38
	s_mov_b32 s6, s62
	v_writelane_b32 v255, s6, 39
	s_movk_i32 s81, 0x7fff
	s_mov_b32 s57, 0x41000000
	v_writelane_b32 v255, s7, 40
	s_mov_b32 s6, s66
	v_writelane_b32 v255, s6, 41
	s_movk_i32 s33, 0xfefe
	s_mov_b32 s85, 0x900000
	v_writelane_b32 v255, s7, 42
	v_writelane_b32 v255, s76, 43
	v_writelane_b32 v255, s84, 44
	s_mov_b32 s72, 0xc0e00000
	s_mov_b32 s73, 0
	s_mov_b32 s71, 0
	s_mov_b64 s[4:5], -1
	s_mov_b64 s[78:79], 0x80
	s_mov_b32 s82, 0x3e38aa3b
	s_mov_b32 s88, 0xc01d265f
	s_mov_b32 s50, s69
	s_mov_b32 s86, s68
	s_mov_b32 s60, s49
	v_writelane_b32 v255, s87, 45
	s_branch .LBB0_314

.LBB0_561:
	s_and_b64 vcc, exec, s[16:17]
	s_cbranch_vccz .LBB0_711
	v_readlane_b32 s6, v254, 50
	v_readlane_b32 s7, v254, 46
	s_mul_i32 s6, s35, s6
	s_sub_i32 s7, s7, s36
	s_add_i32 s23, s7, s6
	s_lshl_b32 s22, s35, 3
	s_mov_b64 s[6:7], -1
	s_and_b64 vcc, exec, s[90:91]
	s_cbranch_vccz .LBB0_637
	v_mbcnt_lo_u32_b32 v66, -1, 0
	v_mbcnt_hi_u32_b32 v66, -1, v66
	s_getreg_b32 s6, hwreg(HW_REG_HW_ID, 0, 6)
	s_lshl_b32 s6, s6, 2
	s_and_b32 s6, s6, 0xfc
	s_or_b32 s6, s6, 0x27100
	v_mov_b32_e32 v0, s6
	ds_read_b32 v0, v0
	s_cmpk_gt_i32 s23, 0x9
	s_waitcnt lgkmcnt(0)
	v_readfirstlane_b32 s9, v0
	s_cbranch_scc1 .LBB0_636
	s_add_i32 s20, s23, 0xe0d
	s_mul_hi_i32 s6, s20, 0x2aaaaaab
	s_lshr_b32 s7, s6, 31
	s_ashr_i32 s15, s6, 9
	s_add_i32 s15, s15, s7
	s_mul_i32 s16, s15, 0xfffff400
	s_add_i32 s16, s16, s20
	s_cmpk_gt_i32 s16, 0x7ff
	s_mov_b64 s[12:13], -1
	s_cbranch_scc0 .LBB0_566
	s_add_i32 s6, s16, 0xfffff800
	s_mov_b32 s10, 31
	s_lshl_b32 s7, s15, 5
	s_lshr_b32 s6, s6, 5
	s_lshl_b32 s24, s20, 8
	s_ashr_i32 s11, s10, 31
	s_add_i32 s6, s6, s7
	s_lshl_b32 s14, s20, 5
	s_and_b32 s8, s24, 0x300
	s_lshl_b64 s[10:11], s[10:11], 3
	s_add_u32 s10, s0, s10
	s_addc_u32 s11, s1, s11
	s_load_dwordx2 s[10:11], s[10:11], 0x0
	s_ashr_i32 s7, s6, 31
	s_lshl_b64 s[12:13], s[6:7], 20
	s_lshl_b64 s[6:7], s[6:7], 22
	s_waitcnt lgkmcnt(0)
	s_add_u32 s6, s10, s6
	s_mov_b32 s10, 35
	s_addc_u32 s7, s11, s7
	s_ashr_i32 s11, s10, 31
	s_lshl_b64 s[10:11], s[10:11], 3
	s_add_u32 s10, s0, s10
	s_addc_u32 s11, s1, s11
	s_load_dwordx2 s[10:11], s[10:11], 0x0
	s_waitcnt lgkmcnt(0)
	s_add_u32 s10, s10, s12
	s_addc_u32 s11, s11, s13
	s_add_u32 s10, s10, 0x12800000
	s_addc_u32 s11, s11, 0
	s_mov_b64 s[12:13], 0

.LBB0_569:
	v_lshl_or_b32 v67, s9, 6, v66
	v_ashrrev_i32_e32 v69, 6, v67
	s_and_b32 s14, s14, 0x380
	v_lshlrev_b32_e32 v135, 4, v69
	v_add_u32_e32 v0, s14, v135
	s_waitcnt vmcnt(0)
	v_mad_i64_i32 v[2:3], s[16:17], s12, v0, 0
	v_and_b32_e32 v68, 63, v66
	v_lshl_add_u64 v[2:3], v[2:3], 2, s[6:7]
	s_mov_b32 s9, s71
	v_lshl_add_u64 v[2:3], s[8:9], 2, v[2:3]
	v_lshlrev_b32_e32 v0, 4, v68
	v_lshl_add_u64 v[2:3], v[2:3], 0, v[0:1]
	s_lshl_b32 s70, s12, 2
	v_lshl_add_u64 v[10:11], v[2:3], 0, s[70:71]
	global_load_dwordx4 v[2:5], v[2:3], off nt
	s_nop 0
	global_load_dwordx4 v[6:9], v[10:11], off nt
	v_lshl_add_u64 v[10:11], v[10:11], 0, s[70:71]
	v_lshl_add_u64 v[18:19], v[10:11], 0, s[70:71]
	global_load_dwordx4 v[10:13], v[10:11], off nt
	s_nop 0
	global_load_dwordx4 v[14:17], v[18:19], off nt
	v_lshl_add_u64 v[18:19], v[18:19], 0, s[70:71]
	v_lshl_add_u64 v[26:27], v[18:19], 0, s[70:71]
	global_load_dwordx4 v[18:21], v[18:19], off nt
	s_nop 0
	global_load_dwordx4 v[22:25], v[26:27], off nt
	v_lshl_add_u64 v[26:27], v[26:27], 0, s[70:71]
	v_lshl_add_u64 v[34:35], v[26:27], 0, s[70:71]
	v_lshl_add_u64 v[38:39], v[34:35], 0, s[70:71]
	v_lshl_add_u64 v[42:43], v[38:39], 0, s[70:71]
	v_lshl_add_u64 v[46:47], v[42:43], 0, s[70:71]
	v_lshl_add_u64 v[50:51], v[46:47], 0, s[70:71]
	v_lshl_add_u64 v[54:55], v[50:51], 0, s[70:71]
	v_lshl_add_u64 v[58:59], v[54:55], 0, s[70:71]
	v_lshl_add_u64 v[62:63], v[58:59], 0, s[70:71]
	global_load_dwordx4 v[26:29], v[26:27], off nt
	s_nop 0
	global_load_dwordx4 v[30:33], v[34:35], off nt
	v_lshlrev_b32_e32 v134, 2, v68
	global_load_dwordx4 v[34:37], v[38:39], off nt
	v_lshl_add_u32 v0, v68, 9, 0
	global_load_dwordx4 v[38:41], v[42:43], off nt
	v_bitop3_b32 v68, v69, v66, 7 bitop3:0x78
	global_load_dwordx4 v[42:45], v[46:47], off nt
	v_lshrrev_b32_e32 v69, 5, v67
	global_load_dwordx4 v[46:49], v[50:51], off nt
	v_xor_b32_e32 v69, v69, v66
	global_load_dwordx4 v[50:53], v[54:55], off nt
	v_readlane_b32 s6, v254, 44
	global_load_dwordx4 v[54:57], v[58:59], off nt
	v_lshlrev_b32_e32 v69, 4, v69
	global_load_dwordx4 v[58:61], v[62:63], off nt
	v_lshl_add_u64 v[62:63], v[62:63], 0, s[70:71]
	global_load_dwordx4 v[62:65], v[62:63], off nt
	v_ashrrev_i32_e32 v140, 3, v67
	v_add_u32_e32 v70, 0x200, v67
	v_add_u32_e32 v71, 0x400, v67
	v_add_u32_e32 v67, 0x600, v67
	s_mul_i32 s26, s6, s35
	v_readlane_b32 s6, v254, 48
	v_and_b32_e32 v69, 0x70, v69
	v_lshlrev_b32_e32 v66, 4, v66
	v_ashrrev_i32_e32 v141, 3, v70
	v_ashrrev_i32_e32 v142, 3, v71
	v_ashrrev_i32_e32 v143, 3, v67
	s_mul_i32 s29, s6, s35
	v_readlane_b32 s6, v254, 51
	v_lshlrev_b32_e32 v68, 4, v68
	v_add_u32_e32 v69, 0, v69
	v_and_b32_e32 v136, 0x70, v66
	v_lshlrev_b32_e32 v66, 7, v140
	v_lshlrev_b32_e32 v70, 7, v141
	v_lshlrev_b32_e32 v71, 7, v142
	v_lshlrev_b32_e32 v67, 7, v143
	s_mul_i32 s6, s6, s35
	v_mov_b32_e32 v137, v1
	s_lshl_b32 s25, s35, 12
	s_lshl_b32 s27, s35, 4
	s_lshl_b32 s28, s35, 8
	s_add_i32 s30, s6, 0xded
	v_add_u32_e32 v144, v0, v68
	v_add_u32_e32 v145, v69, v66
	v_add_u32_e32 v146, v69, v70
	v_add_u32_e32 v147, v69, v71
	v_add_u32_e32 v148, v69, v67
	v_readlane_b32 s36, v254, 47
	s_mov_b32 s70, s14
	s_mov_b32 s37, s31
	s_mov_b32 s12, s8
	s_mov_b64 s[16:17], s[10:11]
	s_branch .LBB0_573

.LBB0_573:
	v_readlane_b32 s6, v254, 46
	s_add_i32 s6, s6, s29
	s_add_i32 s9, s20, s22
	s_add_i32 s7, s6, 0xded
	s_cmpk_lt_i32 s7, 0xe17
	s_cselect_b64 s[18:19], -1, 0
	s_cmpk_gt_i32 s7, 0xe16
	s_cbranch_scc1 .LBB0_580
	s_mul_hi_i32 s7, s7, 0x2aaaaaab
	s_lshr_b32 s12, s7, 31
	s_ashr_i32 s20, s7, 9
	s_add_i32 s20, s20, s12
	s_mul_i32 s7, s20, 0xfffff400
	s_add_i32 s37, s6, s7
	s_add_i32 s21, s37, 0xded
	s_cmpk_gt_i32 s21, 0x7ff
	s_mov_b64 s[14:15], -1
	s_cbranch_scc0 .LBB0_576
	s_addk_i32 s37, 0x5ed
	s_mov_b32 s14, 31
	s_lshl_b32 s6, s20, 5
	s_lshr_b32 s7, s37, 5
	s_ashr_i32 s15, s14, 31
	s_add_i32 s6, s7, s6
	s_lshl_b32 s13, s9, 5
	s_and_b32 s12, s24, 0x300
	s_lshl_b64 s[14:15], s[14:15], 3
	s_add_u32 s14, s0, s14
	s_addc_u32 s15, s1, s15
	s_load_dwordx2 s[14:15], s[14:15], 0x0
	s_ashr_i32 s7, s6, 31
	s_lshl_b64 s[16:17], s[6:7], 20
	s_lshl_b64 s[6:7], s[6:7], 22
	s_waitcnt lgkmcnt(0)
	s_add_u32 s6, s14, s6
	s_mov_b32 s14, 35
	s_addc_u32 s7, s15, s7
	s_ashr_i32 s15, s14, 31
	s_lshl_b64 s[14:15], s[14:15], 3
	s_add_u32 s14, s0, s14
	s_addc_u32 s15, s1, s15
	s_load_dwordx2 s[14:15], s[14:15], 0x0
	s_waitcnt lgkmcnt(0)
	s_add_u32 s14, s14, s16
	s_addc_u32 s15, s15, s17
	s_add_u32 s16, s14, 0x12800000
	s_addc_u32 s17, s15, 0
	s_mov_b64 s[14:15], 0

.LBB0_604:
	v_ashrrev_i32_e32 v139, 31, v138
	v_lshlrev_b64 v[138:139], 10, v[138:139]
	v_lshl_add_u64 v[138:139], s[10:11], 0, v[138:139]
	v_lshl_add_u64 v[138:139], v[138:139], 0, s[70:71]
	v_lshl_add_u64 v[138:139], v[138:139], 0, v[136:137]
	s_andn2_b64 vcc, exec, s[18:19]
	s_mov_b64 s[6:7], -1
	s_waitcnt lgkmcnt(0)
	global_store_dwordx4 v[138:139], v[130:133], off nt
	s_cbranch_vccnz .LBB0_572
	v_readlane_b32 s6, v254, 46
	s_add_i32 s6, s6, s26
	s_add_i32 s20, s9, s22
	s_add_i32 s7, s6, 0xded
	s_cmpk_gt_i32 s7, 0xe16
	s_cbranch_scc1 .LBB0_612
	s_mul_hi_i32 s7, s7, 0x2aaaaaab
	s_lshr_b32 s8, s7, 31
	s_ashr_i32 s13, s7, 9
	s_add_i32 s13, s13, s8
	s_mul_i32 s7, s13, 0xfffff400
	s_add_i32 s21, s6, s7
	s_add_i32 s15, s21, 0xded
	s_cmpk_gt_i32 s15, 0x7ff
	s_mov_b64 s[18:19], -1
	s_cbranch_scc0 .LBB0_608
	s_addk_i32 s21, 0x525
	s_mov_b32 s10, 31
	s_lshl_b32 s6, s13, 5
	s_lshr_b32 s7, s21, 5
	s_ashr_i32 s11, s10, 31
	s_add_i32 s6, s7, s6
	s_lshl_b32 s9, s20, 5
	s_and_b32 s8, s24, 0x300
	s_lshl_b64 s[10:11], s[10:11], 3
	s_add_u32 s10, s0, s10
	s_addc_u32 s11, s1, s11
	s_load_dwordx2 s[10:11], s[10:11], 0x0
	s_ashr_i32 s7, s6, 31
	s_lshl_b64 s[18:19], s[6:7], 20
	s_lshl_b64 s[6:7], s[6:7], 22
	s_waitcnt lgkmcnt(0)
	s_add_u32 s6, s10, s6
	s_mov_b32 s10, 35
	s_addc_u32 s7, s11, s7
	s_ashr_i32 s11, s10, 31
	s_lshl_b64 s[10:11], s[10:11], 3
	s_add_u32 s10, s0, s10
	s_addc_u32 s11, s1, s11
	s_load_dwordx2 s[10:11], s[10:11], 0x0
	s_waitcnt lgkmcnt(0)
	s_add_u32 s10, s10, s18
	s_addc_u32 s11, s11, s19
	s_add_u32 s10, s10, 0x12800000
	s_addc_u32 s11, s11, 0
	s_mov_b64 s[18:19], 0

.LBB0_1405:
	s_andn2_b64 vcc, exec, s[6:7]
	s_cbranch_vccnz .LBB0_1479
	v_mbcnt_lo_u32_b32 v66, -1, 0
	v_mbcnt_hi_u32_b32 v66, -1, v66
	s_getreg_b32 s6, hwreg(HW_REG_HW_ID, 0, 6)
	s_lshl_b32 s6, s6, 2
	s_and_b32 s6, s6, 0xfc
	s_or_b32 s6, s6, 0x27100
	v_mov_b32_e32 v0, s6
	ds_read_b32 v0, v0
	v_readlane_b32 s6, v254, 50
	v_readlane_b32 s7, v254, 46
	s_mul_i32 s6, s37, s6
	s_sub_i32 s7, s7, s40
	s_add_i32 s6, s7, s6
	s_cmpk_gt_i32 s6, 0x3e7
	s_waitcnt lgkmcnt(0)
	v_readfirstlane_b32 s9, v0
	s_cbranch_scc1 .LBB0_1479
	s_add_i32 s20, s6, 0xa25
	s_mul_hi_i32 s6, s20, 0x2aaaaaab
	s_lshr_b32 s7, s6, 31
	s_ashr_i32 s15, s6, 9
	s_add_i32 s15, s15, s7
	s_mul_i32 s16, s15, 0xfffff400
	s_add_i32 s16, s16, s20
	s_cmpk_gt_i32 s16, 0x7ff
	s_mov_b64 s[12:13], -1
	s_cbranch_scc0 .LBB0_1409
	s_add_i32 s6, s16, 0xfffff800
	s_mov_b32 s10, 31
	s_lshl_b32 s7, s15, 5
	s_lshr_b32 s6, s6, 5
	s_lshl_b32 s22, s20, 8
	s_ashr_i32 s11, s10, 31
	s_add_i32 s6, s6, s7
	s_lshl_b32 s14, s20, 5
	s_and_b32 s8, s22, 0x300
	s_lshl_b64 s[10:11], s[10:11], 3
	s_add_u32 s10, s0, s10
	s_addc_u32 s11, s1, s11
	s_load_dwordx2 s[10:11], s[10:11], 0x0
	s_ashr_i32 s7, s6, 31
	s_lshl_b64 s[12:13], s[6:7], 20
	s_lshl_b64 s[6:7], s[6:7], 22
	s_waitcnt lgkmcnt(0)
	s_add_u32 s6, s10, s6
	s_mov_b32 s10, 35
	s_addc_u32 s7, s11, s7
	s_ashr_i32 s11, s10, 31
	s_lshl_b64 s[10:11], s[10:11], 3
	s_add_u32 s10, s0, s10
	s_addc_u32 s11, s1, s11
	s_load_dwordx2 s[10:11], s[10:11], 0x0
	s_waitcnt lgkmcnt(0)
	s_add_u32 s10, s10, s12
	s_addc_u32 s11, s11, s13
	s_add_u32 s10, s10, 0x12800000
	s_addc_u32 s11, s11, 0
	s_mov_b64 s[12:13], 0

.LBB0_1414:
	v_ashrrev_i32_e32 v139, 31, v138
	v_lshlrev_b64 v[138:139], 10, v[138:139]
	s_add_i32 s31, s31, s26
	v_readlane_b32 s6, v254, 46
	v_lshl_add_u64 v[138:139], s[16:17], 0, v[138:139]
	s_add_i32 s22, s22, s24
	s_add_i32 s25, s25, s26
	s_add_i32 s35, s35, s28
	s_add_i32 s29, s29, s26
	s_add_i32 s6, s6, s31
	v_lshl_add_u64 v[138:139], v[138:139], 0, s[14:15]
	s_cmpk_gt_i32 s6, 0xe0c
	v_lshl_add_u64 v[138:139], v[138:139], 0, v[136:137]
	s_cselect_b64 s[6:7], -1, 0
	s_waitcnt lgkmcnt(0)
	global_store_dwordx4 v[138:139], v[130:133], off nt

.LBB0_1416:
	v_readlane_b32 s6, v254, 46
	s_add_i32 s6, s6, s29
	s_add_i32 s9, s20, s23
	s_add_i32 s7, s6, 0xa05
	s_cmpk_lt_i32 s7, 0xe0d
	s_cselect_b64 s[18:19], -1, 0
	s_cmpk_gt_i32 s7, 0xe0c
	s_cbranch_scc1 .LBB0_1423
	s_mul_hi_i32 s7, s7, 0x2aaaaaab
	s_lshr_b32 s12, s7, 31
	s_ashr_i32 s20, s7, 9
	s_add_i32 s20, s20, s12
	s_mul_i32 s7, s20, 0xfffff400
	s_add_i32 s37, s6, s7
	s_add_i32 s21, s37, 0xa05
	s_cmpk_gt_i32 s21, 0x7ff
	s_mov_b64 s[14:15], -1
	s_cbranch_scc0 .LBB0_1419
	s_addk_i32 s37, 0x205
	s_mov_b32 s14, 31
	s_lshl_b32 s6, s20, 5
	s_lshr_b32 s7, s37, 5
	s_ashr_i32 s15, s14, 31
	s_add_i32 s6, s7, s6
	s_lshl_b32 s13, s9, 5
	s_and_b32 s12, s22, 0x300
	s_lshl_b64 s[14:15], s[14:15], 3
	s_add_u32 s14, s0, s14
	s_addc_u32 s15, s1, s15
	s_load_dwordx2 s[14:15], s[14:15], 0x0
	s_ashr_i32 s7, s6, 31
	s_lshl_b64 s[16:17], s[6:7], 20
	s_lshl_b64 s[6:7], s[6:7], 22
	s_waitcnt lgkmcnt(0)
	s_add_u32 s6, s14, s6
	s_mov_b32 s14, 35
	s_addc_u32 s7, s15, s7
	s_ashr_i32 s15, s14, 31
	s_lshl_b64 s[14:15], s[14:15], 3
	s_add_u32 s14, s0, s14
	s_addc_u32 s15, s1, s15
	s_load_dwordx2 s[14:15], s[14:15], 0x0
	s_waitcnt lgkmcnt(0)
	s_add_u32 s14, s14, s16
	s_addc_u32 s15, s15, s17
	s_add_u32 s16, s14, 0x12800000
	s_addc_u32 s17, s15, 0
	s_mov_b64 s[14:15], 0

.LBB0_1447:
	v_ashrrev_i32_e32 v139, 31, v138
	v_lshlrev_b64 v[138:139], 10, v[138:139]
	v_lshl_add_u64 v[138:139], s[10:11], 0, v[138:139]
	v_lshl_add_u64 v[138:139], v[138:139], 0, s[70:71]
	v_lshl_add_u64 v[138:139], v[138:139], 0, v[136:137]
	s_andn2_b64 vcc, exec, s[18:19]
	s_mov_b64 s[6:7], -1
	s_waitcnt lgkmcnt(0)
	global_store_dwordx4 v[138:139], v[130:133], off nt
	s_cbranch_vccnz .LBB0_1415
	v_readlane_b32 s6, v254, 46
	s_add_i32 s6, s6, s25
	s_add_i32 s20, s9, s23
	s_add_i32 s7, s6, 0xa05
	s_cmpk_gt_i32 s7, 0xe0c
	s_cbranch_scc1 .LBB0_1455
	s_mul_hi_i32 s7, s7, 0x2aaaaaab
	s_lshr_b32 s8, s7, 31
	s_ashr_i32 s13, s7, 9
	s_add_i32 s13, s13, s8
	s_mul_i32 s7, s13, 0xfffff400
	s_add_i32 s21, s6, s7
	s_add_i32 s15, s21, 0xa05
	s_cmpk_gt_i32 s15, 0x7ff
	s_mov_b64 s[18:19], -1
	s_cbranch_scc0 .LBB0_1451
	s_addk_i32 s21, 0x205
	s_mov_b32 s10, 31
	s_lshl_b32 s6, s13, 5
	s_lshr_b32 s7, s21, 5
	s_ashr_i32 s11, s10, 31
	s_add_i32 s6, s7, s6
	s_lshl_b32 s9, s20, 5
	s_and_b32 s8, s22, 0x300
	s_lshl_b64 s[10:11], s[10:11], 3
	s_add_u32 s10, s0, s10
	s_addc_u32 s11, s1, s11
	s_load_dwordx2 s[10:11], s[10:11], 0x0
	s_ashr_i32 s7, s6, 31
	s_lshl_b64 s[18:19], s[6:7], 20
	s_lshl_b64 s[6:7], s[6:7], 22
	s_waitcnt lgkmcnt(0)
	s_add_u32 s6, s10, s6
	s_mov_b32 s10, 35
	s_addc_u32 s7, s11, s7
	s_ashr_i32 s11, s10, 31
	s_lshl_b64 s[10:11], s[10:11], 3
	s_add_u32 s10, s0, s10
	s_addc_u32 s11, s1, s11
	s_load_dwordx2 s[10:11], s[10:11], 0x0
	s_waitcnt lgkmcnt(0)
	s_add_u32 s10, s10, s18
	s_addc_u32 s11, s11, s19
	s_add_u32 s10, s10, 0x12800000
	s_addc_u32 s11, s11, 0
	s_mov_b64 s[18:19], 0
